# nt hint on the remaining one-pass read streams: x->bf16 prologue loads and the out-GEMM residual loads
# baseline (speedup 1.0000x reference)
; __device__ __forceinline__ unsigned pk2(float lo, float hi) { return hw_pk_bf16(lo, hi); }
; __device__ __forceinline__ void p0_prologue(const Frame& F, const Args& a_) {
;     ...
;     { const f32x4* x4 = (const f32x4*)a.in[0]; u32x2* o = (u32x2*)(ws + WS_XB);
;       for (size_t i = gt; i < (size_t)T * D / 4; i += NGT) { const f32x4 v = x4[i]; u32x2 w; w.x = pk2(v.x, v.y); w.y = pk2(v.z, v.w); o[i] = w; } }
.LBB0_9:
	global_load_dwordx4 v[8:11], v[4:5], off nt
	v_lshl_add_u64 v[6:7], v[6:7], 0, s[22:23]
	v_cmp_lt_u64_e32 vcc, s[14:15], v[6:7]
	v_lshl_add_u64 v[4:5], v[4:5], 0, s[10:11]
	s_or_b64 s[12:13], vcc, s[12:13]
	s_waitcnt vmcnt(0)
	v_cvt_pk_bf16_f32 v8, v8, v9
	v_cvt_pk_bf16_f32 v9, v10, v11
	global_store_dwordx2 v[2:3], v[8:9], off
	v_lshl_add_u64 v[2:3], v[2:3], 0, s[6:7]
	s_andn2_b64 exec, exec, s[12:13]
	s_cbranch_execnz .LBB0_9

; __device__ __forceinline__ unsigned cvt_pk_bf16(float lo, float hi) { typedef __bf16 bf16x2_t __attribute__((ext_vector_type(2))); f32x2 v = {lo, hi}; bf16x2_t b = __builtin_convertvector(v, bf16x2_t); return __builtin_bit_cast(unsigned, b); }
;     __device__ __forceinline__ void operator()(const f32x4 (&acc)[2][2][4][2], const Unit& u, int wr, int wc, int fr, int fq) const {
;         const int row0 = u.pm * BM + wr * 64 + fr, col0 = u.pn * BM + wc * 64 + 16 * fq;
; #pragma unroll
;         for (int ai = 0; ai < 2; ++ai)
; #pragma unroll
;             for (int m = 0; m < 4; ++m) { const size_t off = (size_t)(row0 + ai * HALF + m * 16) * ldc + col0;
;                 const u32x4 ra = *(const u32x4*)(R + off), rb = *(const u32x4*)(R + off + 8);
;                 const f32x4 v0 = acc[ai][0][m][0], v1 = acc[ai][0][m][1], v2 = acc[ai][1][m][0], v3 = acc[ai][1][m][1];
;                 u32x4 wa, wb;
;                 wa.x = cvt_pk_bf16(bflo(ra.x) * alpha + v0[0], bfhi(ra.x) * alpha + v0[1]); wa.y = cvt_pk_bf16(bflo(ra.y) * alpha + v0[2], bfhi(ra.y) * alpha + v0[3]);
;                 wa.z = cvt_pk_bf16(bflo(ra.z) * alpha + v1[0], bfhi(ra.z) * alpha + v1[1]); wa.w = cvt_pk_bf16(bflo(ra.w) * alpha + v1[2], bfhi(ra.w) * alpha + v1[3]);
;                 wb.x = cvt_pk_bf16(bflo(rb.x) * alpha + v2[0], bfhi(rb.x) * alpha + v2[1]); wb.y = cvt_pk_bf16(bflo(rb.y) * alpha + v2[2], bfhi(rb.y) * alpha + v2[3]);
;                 wb.z = cvt_pk_bf16(bflo(rb.z) * alpha + v3[0], bfhi(rb.z) * alpha + v3[1]); wb.w = cvt_pk_bf16(bflo(rb.w) * alpha + v3[2], bfhi(rb.w) * alpha + v3[3]);
;                 *(u32x4*)(O + off) = wa; *(u32x4*)(O + off + 8) = wb; }
.LBB0_732:
	v_lshl_add_u32 v132, s60, 8, v237
	v_lshl_add_u32 v130, s73, 8, v239
	v_ashrrev_i32_e32 v133, 31, v132
	v_ashrrev_i32_e32 v131, 31, v130
	v_lshlrev_b64 v[128:129], 11, v[132:133]
	v_lshl_add_u64 v[128:129], v[128:129], 0, v[130:131]
	v_lshlrev_b64 v[128:129], 1, v[128:129]
	v_lshl_add_u64 v[138:139], s[46:47], 0, v[128:129]
	global_load_dwordx4 v[144:147], v[138:139], off offset:16 nt
	global_load_dwordx4 v[148:151], v[138:139], off nt
	s_mov_b64 s[8:9], 0x10000
	v_lshl_add_u64 v[244:245], v[138:139], 0, s[8:9]
	global_load_dwordx4 v[152:155], v[244:245], off offset:16 nt
	global_load_dwordx4 v[156:159], v[244:245], off nt
	s_mov_b64 s[8:9], 0x20000
	v_lshl_add_u64 v[244:245], v[138:139], 0, s[8:9]
	global_load_dwordx4 v[160:163], v[244:245], off offset:16 nt
	global_load_dwordx4 v[164:167], v[244:245], off nt
	s_mov_b64 s[8:9], 0x30000
	v_lshl_add_u64 v[244:245], v[138:139], 0, s[8:9]
	global_load_dwordx4 v[168:171], v[244:245], off offset:16 nt
	global_load_dwordx4 v[172:175], v[244:245], off nt
	s_mov_b64 s[8:9], 0x80000
	v_lshl_add_u64 v[244:245], v[138:139], 0, s[8:9]
	global_load_dwordx4 v[176:179], v[244:245], off offset:16 nt
	global_load_dwordx4 v[180:183], v[244:245], off nt
	s_mov_b64 s[8:9], 0x90000
	v_lshl_add_u64 v[244:245], v[138:139], 0, s[8:9]
	global_load_dwordx4 v[184:187], v[244:245], off offset:16 nt
	global_load_dwordx4 v[188:191], v[244:245], off nt
	s_mov_b64 s[8:9], 0xa0000
	v_lshl_add_u64 v[246:247], v[138:139], 0, s[8:9]
	s_mov_b64 s[8:9], 0xb0000
	v_lshl_add_u64 v[248:249], v[138:139], 0, s[8:9]
	s_nop 0
	s_mov_b64 s[8:9], 0x80000
	s_andn2_b64 vcc, exec, s[36:37]
	s_waitcnt vmcnt(10)
	v_mov_b64_e32 v[134:135], v[144:145]
	v_mov_b64_e32 v[136:137], v[146:147]
	v_mov_b64_e32 v[138:139], v[148:149]
	v_mov_b64_e32 v[140:141], v[150:151]
	v_lshlrev_b32_e32 v142, 16, v138
	v_and_b32_e32 v143, 0xffff0000, v138
	v_lshlrev_b32_e32 v138, 16, v139
	v_and_b32_e32 v139, 0xffff0000, v139
	v_pk_fma_f32 v[124:125], v[142:143], s[70:71], v[124:125] op_sel_hi:[1,0,1]
	v_pk_fma_f32 v[126:127], v[138:139], s[70:71], v[126:127] op_sel_hi:[1,0,1]
	v_cvt_pk_bf16_f32 v124, v124, v125
	v_cvt_pk_bf16_f32 v125, v126, v127
	v_lshlrev_b32_e32 v126, 16, v140
	v_and_b32_e32 v127, 0xffff0000, v140
	v_pk_fma_f32 v[120:121], v[126:127], s[70:71], v[120:121] op_sel_hi:[1,0,1]
	s_nop 0
	v_cvt_pk_bf16_f32 v126, v120, v121
	v_lshlrev_b32_e32 v120, 16, v141
	v_and_b32_e32 v121, 0xffff0000, v141
	v_pk_fma_f32 v[120:121], v[120:121], s[70:71], v[122:123] op_sel_hi:[1,0,1]
	s_nop 0
	v_cvt_pk_bf16_f32 v127, v120, v121
	v_lshlrev_b32_e32 v120, 16, v134
	v_and_b32_e32 v121, 0xffff0000, v134
	v_pk_fma_f32 v[116:117], v[120:121], s[70:71], v[116:117] op_sel_hi:[1,0,1]
	v_lshlrev_b32_e32 v120, 16, v135
	v_and_b32_e32 v121, 0xffff0000, v135
	v_pk_fma_f32 v[118:119], v[120:121], s[70:71], v[118:119] op_sel_hi:[1,0,1]
	v_cvt_pk_bf16_f32 v116, v116, v117
	v_cvt_pk_bf16_f32 v117, v118, v119
	v_lshlrev_b32_e32 v118, 16, v136
	v_and_b32_e32 v119, 0xffff0000, v136
	v_pk_fma_f32 v[112:113], v[118:119], s[70:71], v[112:113] op_sel_hi:[1,0,1]
	s_nop 0
	v_cvt_pk_bf16_f32 v118, v112, v113
	v_lshlrev_b32_e32 v112, 16, v137
	v_and_b32_e32 v113, 0xffff0000, v137
	v_pk_fma_f32 v[112:113], v[112:113], s[70:71], v[114:115] op_sel_hi:[1,0,1]
	s_nop 0
	v_cvt_pk_bf16_f32 v119, v112, v113
	v_lshl_add_u64 v[112:113], s[44:45], 0, v[128:129]
	global_store_dwordx4 v[112:113], v[124:127], off
	global_store_dwordx4 v[112:113], v[116:119], off offset:16
	v_or_b32_e32 v112, 16, v132
	v_ashrrev_i32_e32 v113, 31, v112
	v_lshlrev_b64 v[112:113], 11, v[112:113]
	v_lshl_add_u64 v[112:113], v[112:113], 0, v[130:131]
	v_lshlrev_b64 v[120:121], 1, v[112:113]
	v_lshl_add_u64 v[116:117], s[46:47], 0, v[120:121]
	s_nop 0
	s_waitcnt vmcnt(10)
	v_mov_b64_e32 v[112:113], v[152:153]
	v_mov_b64_e32 v[114:115], v[154:155]
	v_mov_b64_e32 v[116:117], v[156:157]
	v_mov_b64_e32 v[118:119], v[158:159]
	global_load_dwordx4 v[144:147], v[246:247], off offset:16 nt
	global_load_dwordx4 v[148:151], v[246:247], off nt
	global_load_dwordx4 v[152:155], v[248:249], off offset:16 nt
	global_load_dwordx4 v[156:159], v[248:249], off nt
	v_lshlrev_b32_e32 v122, 16, v116
	v_and_b32_e32 v123, 0xffff0000, v116
	v_lshlrev_b32_e32 v116, 16, v117
	v_and_b32_e32 v117, 0xffff0000, v117
	v_pk_fma_f32 v[108:109], v[122:123], s[70:71], v[108:109] op_sel_hi:[1,0,1]
	v_pk_fma_f32 v[110:111], v[116:117], s[70:71], v[110:111] op_sel_hi:[1,0,1]
	v_cvt_pk_bf16_f32 v108, v108, v109
	v_cvt_pk_bf16_f32 v109, v110, v111
	v_lshlrev_b32_e32 v110, 16, v118
	v_and_b32_e32 v111, 0xffff0000, v118
	v_pk_fma_f32 v[104:105], v[110:111], s[70:71], v[104:105] op_sel_hi:[1,0,1]
	s_nop 0
	v_cvt_pk_bf16_f32 v110, v104, v105
	v_lshlrev_b32_e32 v104, 16, v119
	v_and_b32_e32 v105, 0xffff0000, v119
	v_pk_fma_f32 v[104:105], v[104:105], s[70:71], v[106:107] op_sel_hi:[1,0,1]
	s_nop 0
	v_cvt_pk_bf16_f32 v111, v104, v105
	v_lshlrev_b32_e32 v104, 16, v112
	v_and_b32_e32 v105, 0xffff0000, v112
	v_pk_fma_f32 v[100:101], v[104:105], s[70:71], v[100:101] op_sel_hi:[1,0,1]
	v_lshlrev_b32_e32 v104, 16, v113
	v_and_b32_e32 v105, 0xffff0000, v113
	v_pk_fma_f32 v[102:103], v[104:105], s[70:71], v[102:103] op_sel_hi:[1,0,1]
	v_cvt_pk_bf16_f32 v100, v100, v101
	v_cvt_pk_bf16_f32 v101, v102, v103
	v_lshlrev_b32_e32 v102, 16, v114
	v_and_b32_e32 v103, 0xffff0000, v114
	v_pk_fma_f32 v[96:97], v[102:103], s[70:71], v[96:97] op_sel_hi:[1,0,1]
	s_nop 0
	v_cvt_pk_bf16_f32 v102, v96, v97
	v_lshlrev_b32_e32 v96, 16, v115
	v_and_b32_e32 v97, 0xffff0000, v115
	v_pk_fma_f32 v[96:97], v[96:97], s[70:71], v[98:99] op_sel_hi:[1,0,1]
	s_nop 0
	v_cvt_pk_bf16_f32 v103, v96, v97
	v_lshl_add_u64 v[96:97], s[44:45], 0, v[120:121]
	global_store_dwordx4 v[96:97], v[108:111], off
	global_store_dwordx4 v[96:97], v[100:103], off offset:16
	v_or_b32_e32 v96, 32, v132
	v_ashrrev_i32_e32 v97, 31, v96
	v_lshlrev_b64 v[96:97], 11, v[96:97]
	v_lshl_add_u64 v[96:97], v[96:97], 0, v[130:131]
	v_lshlrev_b64 v[104:105], 1, v[96:97]
	v_lshl_add_u64 v[100:101], s[46:47], 0, v[104:105]
	s_nop 0
	s_waitcnt vmcnt(14)
; __device__ __forceinline__ unsigned cvt_pk_bf16(float lo, float hi) { typedef __bf16 bf16x2_t __attribute__((ext_vector_type(2))); f32x2 v = {lo, hi}; bf16x2_t b = __builtin_convertvector(v, bf16x2_t); return __builtin_bit_cast(unsigned, b); }
;     __device__ __forceinline__ void operator()(const f32x4 (&acc)[2][2][4][2], const Unit& u, int wr, int wc, int fr, int fq) const {
;     ...
;             for (int m = 0; m < 4; ++m) { const size_t off = (size_t)(row0 + ai * HALF + m * 16) * ldc + col0;
;                 const u32x4 ra = *(const u32x4*)(R + off), rb = *(const u32x4*)(R + off + 8);
;                 const f32x4 v0 = acc[ai][0][m][0], v1 = acc[ai][0][m][1], v2 = acc[ai][1][m][0], v3 = acc[ai][1][m][1];
;                 u32x4 wa, wb;
;                 wa.x = cvt_pk_bf16(bflo(ra.x) * alpha + v0[0], bfhi(ra.x) * alpha + v0[1]); wa.y = cvt_pk_bf16(bflo(ra.y) * alpha + v0[2], bfhi(ra.y) * alpha + v0[3]);
;                 wa.z = cvt_pk_bf16(bflo(ra.z) * alpha + v1[0], bfhi(ra.z) * alpha + v1[1]); wa.w = cvt_pk_bf16(bflo(ra.w) * alpha + v1[2], bfhi(ra.w) * alpha + v1[3]);
;                 wb.x = cvt_pk_bf16(bflo(rb.x) * alpha + v2[0], bfhi(rb.x) * alpha + v2[1]); wb.y = cvt_pk_bf16(bflo(rb.y) * alpha + v2[2], bfhi(rb.y) * alpha + v2[3]);
;                 wb.z = cvt_pk_bf16(bflo(rb.z) * alpha + v3[0], bfhi(rb.z) * alpha + v3[1]); wb.w = cvt_pk_bf16(bflo(rb.w) * alpha + v3[2], bfhi(rb.w) * alpha + v3[3]);
;                 *(u32x4*)(O + off) = wa; *(u32x4*)(O + off + 8) = wb; }
	v_mov_b64_e32 v[96:97], v[160:161]
	v_mov_b64_e32 v[98:99], v[162:163]
	v_mov_b64_e32 v[100:101], v[164:165]
	v_mov_b64_e32 v[102:103], v[166:167]
	v_lshlrev_b32_e32 v106, 16, v100
	v_and_b32_e32 v107, 0xffff0000, v100
	v_lshlrev_b32_e32 v100, 16, v101
	v_and_b32_e32 v101, 0xffff0000, v101
	v_pk_fma_f32 v[92:93], v[106:107], s[70:71], v[92:93] op_sel_hi:[1,0,1]
	v_pk_fma_f32 v[94:95], v[100:101], s[70:71], v[94:95] op_sel_hi:[1,0,1]
	v_cvt_pk_bf16_f32 v92, v92, v93
	v_cvt_pk_bf16_f32 v93, v94, v95
	v_lshlrev_b32_e32 v94, 16, v102
	v_and_b32_e32 v95, 0xffff0000, v102
	v_pk_fma_f32 v[88:89], v[94:95], s[70:71], v[88:89] op_sel_hi:[1,0,1]
	s_nop 0
	v_cvt_pk_bf16_f32 v94, v88, v89
	v_lshlrev_b32_e32 v88, 16, v103
	v_and_b32_e32 v89, 0xffff0000, v103
	v_pk_fma_f32 v[88:89], v[88:89], s[70:71], v[90:91] op_sel_hi:[1,0,1]
	s_nop 0
	v_cvt_pk_bf16_f32 v95, v88, v89
	v_lshlrev_b32_e32 v88, 16, v96
	v_and_b32_e32 v89, 0xffff0000, v96
	v_pk_fma_f32 v[84:85], v[88:89], s[70:71], v[84:85] op_sel_hi:[1,0,1]
	v_lshlrev_b32_e32 v88, 16, v97
	v_and_b32_e32 v89, 0xffff0000, v97
	v_pk_fma_f32 v[86:87], v[88:89], s[70:71], v[86:87] op_sel_hi:[1,0,1]
	v_cvt_pk_bf16_f32 v84, v84, v85
	v_cvt_pk_bf16_f32 v85, v86, v87
	v_lshlrev_b32_e32 v86, 16, v98
	v_and_b32_e32 v87, 0xffff0000, v98
	v_pk_fma_f32 v[80:81], v[86:87], s[70:71], v[80:81] op_sel_hi:[1,0,1]
	s_nop 0
	v_cvt_pk_bf16_f32 v86, v80, v81
	v_lshlrev_b32_e32 v80, 16, v99
	v_and_b32_e32 v81, 0xffff0000, v99
	v_pk_fma_f32 v[80:81], v[80:81], s[70:71], v[82:83] op_sel_hi:[1,0,1]
	s_nop 0
	v_cvt_pk_bf16_f32 v87, v80, v81
	v_lshl_add_u64 v[80:81], s[44:45], 0, v[104:105]
	global_store_dwordx4 v[80:81], v[92:95], off
	global_store_dwordx4 v[80:81], v[84:87], off offset:16
	v_or_b32_e32 v80, 48, v132
	v_ashrrev_i32_e32 v81, 31, v80
	v_lshlrev_b64 v[80:81], 11, v[80:81]
	v_lshl_add_u64 v[80:81], v[80:81], 0, v[130:131]
	v_lshlrev_b64 v[88:89], 1, v[80:81]
	v_lshl_add_u64 v[84:85], s[46:47], 0, v[88:89]
	s_nop 0
	s_waitcnt vmcnt(14)
	v_mov_b64_e32 v[80:81], v[168:169]
	v_mov_b64_e32 v[82:83], v[170:171]
	v_mov_b64_e32 v[84:85], v[172:173]
	v_mov_b64_e32 v[86:87], v[174:175]
	v_lshlrev_b32_e32 v90, 16, v84
	v_and_b32_e32 v91, 0xffff0000, v84
	v_lshlrev_b32_e32 v84, 16, v85
	v_and_b32_e32 v85, 0xffff0000, v85
	v_pk_fma_f32 v[76:77], v[90:91], s[70:71], v[76:77] op_sel_hi:[1,0,1]
	v_pk_fma_f32 v[78:79], v[84:85], s[70:71], v[78:79] op_sel_hi:[1,0,1]
	v_cvt_pk_bf16_f32 v76, v76, v77
	v_cvt_pk_bf16_f32 v77, v78, v79
	v_lshlrev_b32_e32 v78, 16, v86
	v_and_b32_e32 v79, 0xffff0000, v86
	v_pk_fma_f32 v[72:73], v[78:79], s[70:71], v[72:73] op_sel_hi:[1,0,1]
	s_nop 0
	v_cvt_pk_bf16_f32 v78, v72, v73
	v_lshlrev_b32_e32 v72, 16, v87
	v_and_b32_e32 v73, 0xffff0000, v87
	v_pk_fma_f32 v[72:73], v[72:73], s[70:71], v[74:75] op_sel_hi:[1,0,1]
	s_nop 0
	v_cvt_pk_bf16_f32 v79, v72, v73
	v_lshlrev_b32_e32 v72, 16, v80
	v_and_b32_e32 v73, 0xffff0000, v80
	v_pk_fma_f32 v[68:69], v[72:73], s[70:71], v[68:69] op_sel_hi:[1,0,1]
	v_lshlrev_b32_e32 v72, 16, v81
	v_and_b32_e32 v73, 0xffff0000, v81
	v_pk_fma_f32 v[70:71], v[72:73], s[70:71], v[70:71] op_sel_hi:[1,0,1]
	v_cvt_pk_bf16_f32 v68, v68, v69
	v_cvt_pk_bf16_f32 v69, v70, v71
	v_lshlrev_b32_e32 v70, 16, v82
	v_and_b32_e32 v71, 0xffff0000, v82
	v_pk_fma_f32 v[64:65], v[70:71], s[70:71], v[64:65] op_sel_hi:[1,0,1]
	v_lshl_add_u64 v[72:73], v[128:129], 0, s[8:9]
	v_cvt_pk_bf16_f32 v70, v64, v65
	v_lshlrev_b32_e32 v64, 16, v83
	v_and_b32_e32 v65, 0xffff0000, v83
	v_pk_fma_f32 v[64:65], v[64:65], s[70:71], v[66:67] op_sel_hi:[1,0,1]
	s_mov_b64 s[8:9], 0xa0000
	v_cvt_pk_bf16_f32 v71, v64, v65
	v_lshl_add_u64 v[64:65], s[44:45], 0, v[88:89]
	global_store_dwordx4 v[64:65], v[76:79], off
	global_store_dwordx4 v[64:65], v[68:71], off offset:16
	s_nop 1
	v_lshl_add_u64 v[68:69], s[46:47], 0, v[72:73]
	s_nop 0
	s_waitcnt vmcnt(14)
	v_mov_b64_e32 v[64:65], v[176:177]
	v_mov_b64_e32 v[66:67], v[178:179]
	v_mov_b64_e32 v[68:69], v[180:181]
	v_mov_b64_e32 v[70:71], v[182:183]
	v_lshlrev_b32_e32 v74, 16, v68
	v_and_b32_e32 v75, 0xffff0000, v68
	v_lshlrev_b32_e32 v68, 16, v69
	v_and_b32_e32 v69, 0xffff0000, v69
	v_pk_fma_f32 v[60:61], v[74:75], s[70:71], v[60:61] op_sel_hi:[1,0,1]
	v_pk_fma_f32 v[62:63], v[68:69], s[70:71], v[62:63] op_sel_hi:[1,0,1]
	v_cvt_pk_bf16_f32 v60, v60, v61
	v_cvt_pk_bf16_f32 v61, v62, v63
	v_lshlrev_b32_e32 v62, 16, v70
	v_and_b32_e32 v63, 0xffff0000, v70
	v_pk_fma_f32 v[56:57], v[62:63], s[70:71], v[56:57] op_sel_hi:[1,0,1]
	s_nop 0
	v_cvt_pk_bf16_f32 v62, v56, v57
	v_lshlrev_b32_e32 v56, 16, v71
	v_and_b32_e32 v57, 0xffff0000, v71
	v_pk_fma_f32 v[56:57], v[56:57], s[70:71], v[58:59] op_sel_hi:[1,0,1]
	s_nop 0
	v_cvt_pk_bf16_f32 v63, v56, v57
	v_lshlrev_b32_e32 v56, 16, v64
	v_and_b32_e32 v57, 0xffff0000, v64
	v_pk_fma_f32 v[52:53], v[56:57], s[70:71], v[52:53] op_sel_hi:[1,0,1]
	v_lshlrev_b32_e32 v56, 16, v65
	v_and_b32_e32 v57, 0xffff0000, v65
	v_pk_fma_f32 v[54:55], v[56:57], s[70:71], v[54:55] op_sel_hi:[1,0,1]
	v_cvt_pk_bf16_f32 v52, v52, v53
	v_cvt_pk_bf16_f32 v53, v54, v55
	v_lshlrev_b32_e32 v54, 16, v66
	v_and_b32_e32 v55, 0xffff0000, v66
	v_pk_fma_f32 v[48:49], v[54:55], s[70:71], v[48:49] op_sel_hi:[1,0,1]
	v_lshl_add_u64 v[56:57], v[128:129], 0, s[68:69]
	v_cvt_pk_bf16_f32 v54, v48, v49
	v_lshlrev_b32_e32 v48, 16, v67
	v_and_b32_e32 v49, 0xffff0000, v67
	v_pk_fma_f32 v[48:49], v[48:49], s[70:71], v[50:51] op_sel_hi:[1,0,1]
	s_nop 0
	v_cvt_pk_bf16_f32 v55, v48, v49
	v_lshl_add_u64 v[48:49], s[44:45], 0, v[72:73]
	global_store_dwordx4 v[48:49], v[60:63], off
	global_store_dwordx4 v[48:49], v[52:55], off offset:16
	s_nop 1
	v_lshl_add_u64 v[52:53], s[46:47], 0, v[56:57]
	s_nop 0
	s_waitcnt vmcnt(14)
; #define PG8_BAR __builtin_amdgcn_s_barrier()
; __device__ __forceinline__ unsigned cvt_pk_bf16(float lo, float hi) { typedef __bf16 bf16x2_t __attribute__((ext_vector_type(2))); f32x2 v = {lo, hi}; bf16x2_t b = __builtin_convertvector(v, bf16x2_t); return __builtin_bit_cast(unsigned, b); }
; template <class Epi, class Sched, bool GATHER, bool FP8 = false, bool ALIGN = true>
; __device__ __forceinline__ void gemm_phase(LAS unsigned char* lds, int wave, const Gemm g, const Sched& S, const Epi& E) {
;     ...
;         if (!has_next) break;
; #pragma unroll
;         for (int a = 0; a < 2; ++a)
; #pragma unroll
;             for (int b = 0; b < 2; ++b)
; #pragma unroll
;                 for (int m = 0; m < 4; ++m)
; #pragma unroll
;                     for (int n = 0; n < 2; ++n) acc[a][b][m][n] = (f32x4){0.f, 0.f, 0.f, 0.f};
;         cur = nxt; cB = nB; ++ui;
;         if constexpr (ALIGN) { if (wr == 1) PG8_BAR; }
;     __device__ __forceinline__ void operator()(const f32x4 (&acc)[2][2][4][2], const Unit& u, int wr, int wc, int fr, int fq) const {
;     ...
;             for (int m = 0; m < 4; ++m) { const size_t off = (size_t)(row0 + ai * HALF + m * 16) * ldc + col0;
;                 const u32x4 ra = *(const u32x4*)(R + off), rb = *(const u32x4*)(R + off + 8);
;                 const f32x4 v0 = acc[ai][0][m][0], v1 = acc[ai][0][m][1], v2 = acc[ai][1][m][0], v3 = acc[ai][1][m][1];
;                 u32x4 wa, wb;
;                 wa.x = cvt_pk_bf16(bflo(ra.x) * alpha + v0[0], bfhi(ra.x) * alpha + v0[1]); wa.y = cvt_pk_bf16(bflo(ra.y) * alpha + v0[2], bfhi(ra.y) * alpha + v0[3]);
;                 wa.z = cvt_pk_bf16(bflo(ra.z) * alpha + v1[0], bfhi(ra.z) * alpha + v1[1]); wa.w = cvt_pk_bf16(bflo(ra.w) * alpha + v1[2], bfhi(ra.w) * alpha + v1[3]);
;                 wb.x = cvt_pk_bf16(bflo(rb.x) * alpha + v2[0], bfhi(rb.x) * alpha + v2[1]); wb.y = cvt_pk_bf16(bflo(rb.y) * alpha + v2[2], bfhi(rb.y) * alpha + v2[3]);
;                 wb.z = cvt_pk_bf16(bflo(rb.z) * alpha + v3[0], bfhi(rb.z) * alpha + v3[1]); wb.w = cvt_pk_bf16(bflo(rb.w) * alpha + v3[2], bfhi(rb.w) * alpha + v3[3]);
;                 *(u32x4*)(O + off) = wa; *(u32x4*)(O + off + 8) = wb; }
	v_mov_b64_e32 v[48:49], v[184:185]
	v_mov_b64_e32 v[50:51], v[186:187]
	v_mov_b64_e32 v[52:53], v[188:189]
	v_mov_b64_e32 v[54:55], v[190:191]
	v_lshlrev_b32_e32 v58, 16, v52
	v_and_b32_e32 v59, 0xffff0000, v52
	v_lshlrev_b32_e32 v52, 16, v53
	v_and_b32_e32 v53, 0xffff0000, v53
	v_pk_fma_f32 v[44:45], v[58:59], s[70:71], v[44:45] op_sel_hi:[1,0,1]
	v_pk_fma_f32 v[46:47], v[52:53], s[70:71], v[46:47] op_sel_hi:[1,0,1]
	v_cvt_pk_bf16_f32 v44, v44, v45
	v_cvt_pk_bf16_f32 v45, v46, v47
	v_lshlrev_b32_e32 v46, 16, v54
	v_and_b32_e32 v47, 0xffff0000, v54
	v_pk_fma_f32 v[40:41], v[46:47], s[70:71], v[40:41] op_sel_hi:[1,0,1]
	s_nop 0
	v_cvt_pk_bf16_f32 v46, v40, v41
	v_lshlrev_b32_e32 v40, 16, v55
	v_and_b32_e32 v41, 0xffff0000, v55
	v_pk_fma_f32 v[40:41], v[40:41], s[70:71], v[42:43] op_sel_hi:[1,0,1]
	s_nop 0
	v_cvt_pk_bf16_f32 v47, v40, v41
	v_lshlrev_b32_e32 v40, 16, v48
	v_and_b32_e32 v41, 0xffff0000, v48
	v_pk_fma_f32 v[36:37], v[40:41], s[70:71], v[36:37] op_sel_hi:[1,0,1]
	v_lshlrev_b32_e32 v40, 16, v49
	v_and_b32_e32 v41, 0xffff0000, v49
	v_pk_fma_f32 v[38:39], v[40:41], s[70:71], v[38:39] op_sel_hi:[1,0,1]
	v_cvt_pk_bf16_f32 v36, v36, v37
	v_cvt_pk_bf16_f32 v37, v38, v39
	v_lshlrev_b32_e32 v38, 16, v50
	v_and_b32_e32 v39, 0xffff0000, v50
	v_pk_fma_f32 v[32:33], v[38:39], s[70:71], v[32:33] op_sel_hi:[1,0,1]
	v_lshl_add_u64 v[40:41], v[128:129], 0, s[8:9]
	v_cvt_pk_bf16_f32 v38, v32, v33
	v_lshlrev_b32_e32 v32, 16, v51
	v_and_b32_e32 v33, 0xffff0000, v51
	v_pk_fma_f32 v[32:33], v[32:33], s[70:71], v[34:35] op_sel_hi:[1,0,1]
	s_mov_b64 s[8:9], 0xb0000
	v_cvt_pk_bf16_f32 v39, v32, v33
	v_lshl_add_u64 v[32:33], s[44:45], 0, v[56:57]
	global_store_dwordx4 v[32:33], v[44:47], off
	global_store_dwordx4 v[32:33], v[36:39], off offset:16
	s_nop 1
	v_lshl_add_u64 v[36:37], s[46:47], 0, v[40:41]
	s_nop 0
	s_waitcnt vmcnt(12)
	v_mov_b64_e32 v[32:33], v[144:145]
	v_mov_b64_e32 v[34:35], v[146:147]
	v_mov_b64_e32 v[36:37], v[148:149]
	v_mov_b64_e32 v[38:39], v[150:151]
	v_lshlrev_b32_e32 v42, 16, v36
	v_and_b32_e32 v43, 0xffff0000, v36
	v_lshlrev_b32_e32 v36, 16, v37
	v_and_b32_e32 v37, 0xffff0000, v37
	v_pk_fma_f32 v[28:29], v[42:43], s[70:71], v[28:29] op_sel_hi:[1,0,1]
	v_pk_fma_f32 v[30:31], v[36:37], s[70:71], v[30:31] op_sel_hi:[1,0,1]
	v_cvt_pk_bf16_f32 v28, v28, v29
	v_cvt_pk_bf16_f32 v29, v30, v31
	v_lshlrev_b32_e32 v30, 16, v38
	v_and_b32_e32 v31, 0xffff0000, v38
	v_pk_fma_f32 v[24:25], v[30:31], s[70:71], v[24:25] op_sel_hi:[1,0,1]
	s_nop 0
	v_cvt_pk_bf16_f32 v30, v24, v25
	v_lshlrev_b32_e32 v24, 16, v39
	v_and_b32_e32 v25, 0xffff0000, v39
	v_pk_fma_f32 v[24:25], v[24:25], s[70:71], v[26:27] op_sel_hi:[1,0,1]
	s_nop 0
	v_cvt_pk_bf16_f32 v31, v24, v25
	v_lshlrev_b32_e32 v24, 16, v32
	v_and_b32_e32 v25, 0xffff0000, v32
	v_pk_fma_f32 v[20:21], v[24:25], s[70:71], v[20:21] op_sel_hi:[1,0,1]
	v_lshlrev_b32_e32 v24, 16, v33
	v_and_b32_e32 v25, 0xffff0000, v33
	v_pk_fma_f32 v[22:23], v[24:25], s[70:71], v[22:23] op_sel_hi:[1,0,1]
	v_cvt_pk_bf16_f32 v20, v20, v21
	v_cvt_pk_bf16_f32 v21, v22, v23
	v_lshlrev_b32_e32 v22, 16, v34
	v_and_b32_e32 v23, 0xffff0000, v34
	v_pk_fma_f32 v[16:17], v[22:23], s[70:71], v[16:17] op_sel_hi:[1,0,1]
	v_lshl_add_u64 v[24:25], v[128:129], 0, s[8:9]
	v_cvt_pk_bf16_f32 v22, v16, v17
	v_lshlrev_b32_e32 v16, 16, v35
	v_and_b32_e32 v17, 0xffff0000, v35
	v_pk_fma_f32 v[16:17], v[16:17], s[70:71], v[18:19] op_sel_hi:[1,0,1]
	s_mov_b64 s[8:9], -1
	v_cvt_pk_bf16_f32 v23, v16, v17
	v_lshl_add_u64 v[16:17], s[44:45], 0, v[40:41]
	global_store_dwordx4 v[16:17], v[28:31], off
	global_store_dwordx4 v[16:17], v[20:23], off offset:16
	s_nop 1
	v_lshl_add_u64 v[20:21], s[46:47], 0, v[24:25]
	s_nop 0
	s_waitcnt vmcnt(12)
	v_mov_b64_e32 v[16:17], v[152:153]
	v_mov_b64_e32 v[18:19], v[154:155]
	v_mov_b64_e32 v[20:21], v[156:157]
	v_mov_b64_e32 v[22:23], v[158:159]
	v_lshlrev_b32_e32 v26, 16, v20
	v_and_b32_e32 v27, 0xffff0000, v20
	v_lshlrev_b32_e32 v20, 16, v21
	v_and_b32_e32 v21, 0xffff0000, v21
	v_pk_fma_f32 v[12:13], v[26:27], s[70:71], v[12:13] op_sel_hi:[1,0,1]
	v_pk_fma_f32 v[14:15], v[20:21], s[70:71], v[14:15] op_sel_hi:[1,0,1]
	v_cvt_pk_bf16_f32 v12, v12, v13
	v_cvt_pk_bf16_f32 v13, v14, v15
	v_lshlrev_b32_e32 v14, 16, v22
	v_and_b32_e32 v15, 0xffff0000, v22
	v_pk_fma_f32 v[8:9], v[14:15], s[70:71], v[8:9] op_sel_hi:[1,0,1]
	s_nop 0
	v_cvt_pk_bf16_f32 v14, v8, v9
	v_lshlrev_b32_e32 v8, 16, v23
	v_and_b32_e32 v9, 0xffff0000, v23
	v_pk_fma_f32 v[8:9], v[8:9], s[70:71], v[10:11] op_sel_hi:[1,0,1]
	s_nop 0
	v_cvt_pk_bf16_f32 v15, v8, v9
	v_lshlrev_b32_e32 v8, 16, v16
	v_and_b32_e32 v9, 0xffff0000, v16
	v_pk_fma_f32 v[4:5], v[8:9], s[70:71], v[4:5] op_sel_hi:[1,0,1]
	v_lshlrev_b32_e32 v8, 16, v17
	v_and_b32_e32 v9, 0xffff0000, v17
	v_pk_fma_f32 v[6:7], v[8:9], s[70:71], v[6:7] op_sel_hi:[1,0,1]
	v_cvt_pk_bf16_f32 v4, v4, v5
	v_cvt_pk_bf16_f32 v5, v6, v7
	v_lshlrev_b32_e32 v6, 16, v18
	v_and_b32_e32 v7, 0xffff0000, v18
	v_pk_fma_f32 v[0:1], v[6:7], s[70:71], v[0:1] op_sel_hi:[1,0,1]
	s_nop 0
	v_cvt_pk_bf16_f32 v6, v0, v1
	v_lshlrev_b32_e32 v0, 16, v19
	v_and_b32_e32 v1, 0xffff0000, v19
	v_pk_fma_f32 v[0:1], v[0:1], s[70:71], v[2:3] op_sel_hi:[1,0,1]
	s_nop 0
	v_cvt_pk_bf16_f32 v7, v0, v1
	v_lshl_add_u64 v[0:1], s[44:45], 0, v[24:25]
	global_store_dwordx4 v[0:1], v[12:15], off
	global_store_dwordx4 v[0:1], v[4:7], off offset:16
	s_cbranch_vccnz .LBB0_718
	s_andn2_b64 vcc, exec, s[42:43]
	s_cbranch_vccnz .LBB0_717
	s_barrier
	s_branch .LBB0_717
